# prologue modulation GEMV loop software-pipelined by one trip (two register sets, counted waits): the 384 waves that own those items no longer end the phase late
# speedup vs baseline: 1.0077x; 1.0003x over previous
.Lmod_loop:
	v_add_co_u32_e32 v166, vcc, s3, v18
	v_lshl_add_u64 v[170:171], s[14:15], 0, v[20:21]
	s_nop 0
	v_addc_co_u32_e32 v167, vcc, -1, v19, vcc
	v_lshl_add_u64 v[168:169], s[18:19], 0, v[20:21]
	global_load_dwordx4 v[162:165], v[18:19], off nt
	global_load_dword v161, v[170:171], off
	global_load_dword v195, v[168:169], off
	global_load_dword v197, v[170:171], off offset:32
	global_load_dword v199, v[168:169], off offset:32
	global_load_dword v201, v[170:171], off offset:64
	global_load_dword v203, v[168:169], off offset:64
	global_load_dword v205, v[170:171], off offset:96
	global_load_dword v207, v[168:169], off offset:96
	global_load_dword v209, v[170:171], off offset:128
	global_load_dword v211, v[168:169], off offset:128
	global_load_dword v213, v[170:171], off offset:160
	global_load_dword v215, v[168:169], off offset:160
	global_load_dword v217, v[170:171], off offset:192
	global_load_dword v219, v[168:169], off offset:192
	global_load_dword v221, v[170:171], off offset:224
	global_load_dword v223, v[168:169], off offset:224
	v_add_co_u32_e32 v170, vcc, s4, v170
	global_load_dwordx4 v[166:169], v[166:167], off nt
	s_nop 0
	v_addc_co_u32_e32 v171, vcc, 0, v171, vcc
	v_add_co_u32_e32 v172, vcc, s5, v18
	global_load_dword v225, v[170:171], off
	global_load_dword v226, v[170:171], off offset:32
	global_load_dword v227, v[170:171], off offset:64
	global_load_dword v228, v[170:171], off offset:96
	global_load_dword v229, v[170:171], off offset:128
	global_load_dword v230, v[170:171], off offset:160
	global_load_dword v231, v[170:171], off offset:192
	global_load_dword v232, v[170:171], off offset:224
	s_waitcnt lgkmcnt(0)
	v_addc_co_u32_e32 v173, vcc, -1, v19, vcc
	v_add_co_u32_e32 v174, vcc, s8, v18
	s_add_i32 s2, s2, 8
	s_nop 0
	v_addc_co_u32_e32 v175, vcc, -1, v19, vcc
	v_add_co_u32_e32 v178, vcc, s9, v18
	global_load_dwordx4 v[170:173], v[172:173], off nt
	s_nop 0
	global_load_dwordx4 v[174:177], v[174:175], off nt
	v_addc_co_u32_e32 v179, vcc, -1, v19, vcc
	v_add_co_u32_e32 v182, vcc, s10, v18
	s_add_u32 s14, s14, 0x100
	s_nop 0
	v_addc_co_u32_e32 v183, vcc, -1, v19, vcc
	v_add_co_u32_e32 v186, vcc, s11, v18
	global_load_dwordx4 v[178:181], v[178:179], off nt
	s_nop 0
	global_load_dwordx4 v[182:185], v[182:183], off nt
	v_addc_co_u32_e32 v187, vcc, -1, v19, vcc
	v_add_co_u32_e32 v190, vcc, s20, v18
	s_addc_u32 s15, s15, 0
	s_nop 0
	v_addc_co_u32_e32 v191, vcc, -1, v19, vcc
	global_load_dwordx4 v[186:189], v[186:187], off nt
	s_nop 0
	global_load_dwordx4 v[190:193], v[190:191], off nt
	s_add_u32 s18, s18, 0x100
	s_addc_u32 s19, s19, 0
	s_cmpk_gt_u32 s2, 0xf7
	v_lshl_add_u64 v[18:19], v[18:19], 0, s[0:1]
	s_waitcnt vmcnt(62)
	v_mul_f32_e32 v52, 0xbfb8aa3b, v1
	s_waitcnt vmcnt(61)
	v_mul_f32_e32 v54, 0xbfb8aa3b, v53
	v_exp_f32_e32 v52, v52
	s_waitcnt vmcnt(60)
	v_mul_f32_e32 v56, 0xbfb8aa3b, v55
	s_waitcnt vmcnt(59)
	v_mul_f32_e32 v58, 0xbfb8aa3b, v57
	v_exp_f32_e32 v54, v54
	s_waitcnt vmcnt(58)
	v_mul_f32_e32 v60, 0xbfb8aa3b, v59
	s_waitcnt vmcnt(57)
	v_mul_f32_e32 v62, 0xbfb8aa3b, v61
	v_exp_f32_e32 v56, v56
	v_exp_f32_e32 v58, v58
	s_waitcnt vmcnt(56)
	v_mul_f32_e32 v64, 0xbfb8aa3b, v63
	s_waitcnt vmcnt(55)
	v_mul_f32_e32 v66, 0xbfb8aa3b, v65
	v_exp_f32_e32 v60, v60
	v_exp_f32_e32 v62, v62
	s_waitcnt vmcnt(54)
	v_mul_f32_e32 v68, 0xbfb8aa3b, v67
	s_waitcnt vmcnt(53)
	v_mul_f32_e32 v70, 0xbfb8aa3b, v69
	s_waitcnt vmcnt(45)
	v_mul_f32_e32 v91, 0xbfb8aa3b, v83
	s_waitcnt vmcnt(44)
	v_mul_f32_e32 v92, 0xbfb8aa3b, v84
	v_exp_f32_e32 v91, v91
	s_waitcnt vmcnt(43)
	v_mul_f32_e32 v93, 0xbfb8aa3b, v85
	v_exp_f32_e32 v92, v92
	s_waitcnt vmcnt(42)
	v_mul_f32_e32 v94, 0xbfb8aa3b, v86
	v_exp_f32_e32 v93, v93
	v_exp_f32_e32 v64, v64
	v_exp_f32_e32 v66, v66
	s_waitcnt vmcnt(41)
	v_mul_f32_e32 v95, 0xbfb8aa3b, v87
	v_exp_f32_e32 v94, v94
	v_add_f32_e32 v52, 1.0, v52
	v_mul_f32_e32 v72, 0xbfb8aa3b, v71
	v_mul_f32_e32 v74, 0xbfb8aa3b, v73
	v_exp_f32_e32 v68, v68
	v_exp_f32_e32 v70, v70
	s_waitcnt vmcnt(40)
	v_mul_f32_e32 v96, 0xbfb8aa3b, v88
	v_exp_f32_e32 v95, v95
	v_add_f32_e32 v54, 1.0, v54
	v_rcp_f32_e32 v52, v52
	v_add_f32_e32 v91, 1.0, v91
	v_mul_f32_e32 v76, 0xbfb8aa3b, v75
	v_mul_f32_e32 v78, 0xbfb8aa3b, v77
	v_exp_f32_e32 v72, v72
	v_exp_f32_e32 v74, v74
	s_waitcnt vmcnt(39)
	v_mul_f32_e32 v97, 0xbfb8aa3b, v89
	v_exp_f32_e32 v96, v96
	v_add_f32_e32 v56, 1.0, v56
	v_add_f32_e32 v58, 1.0, v58
	v_rcp_f32_e32 v54, v54
	v_add_f32_e32 v92, 1.0, v92
	v_rcp_f32_e32 v91, v91
	v_mul_f32_e32 v80, 0xbfb8aa3b, v79
	v_mul_f32_e32 v82, 0xbfb8aa3b, v81
	v_exp_f32_e32 v76, v76
	v_exp_f32_e32 v78, v78
	s_waitcnt vmcnt(38)
	v_mul_f32_e32 v98, 0xbfb8aa3b, v90
	v_exp_f32_e32 v97, v97
	v_add_f32_e32 v60, 1.0, v60
	v_add_f32_e32 v62, 1.0, v62
	v_rcp_f32_e32 v56, v56
	v_rcp_f32_e32 v58, v58
	v_add_f32_e32 v93, 1.0, v93
	v_rcp_f32_e32 v92, v92
	v_exp_f32_e32 v80, v80
	v_exp_f32_e32 v82, v82
	v_exp_f32_e32 v98, v98
	v_add_f32_e32 v64, 1.0, v64
	v_add_f32_e32 v66, 1.0, v66
	v_rcp_f32_e32 v60, v60
	v_rcp_f32_e32 v62, v62
	v_add_f32_e32 v94, 1.0, v94
	v_rcp_f32_e32 v93, v93
	v_add_f32_e32 v68, 1.0, v68
	v_add_f32_e32 v70, 1.0, v70
	v_rcp_f32_e32 v64, v64
	v_rcp_f32_e32 v66, v66
	v_add_f32_e32 v95, 1.0, v95
	v_rcp_f32_e32 v94, v94
	v_mul_f32_e32 v52, v1, v52
	v_add_f32_e32 v72, 1.0, v72
	v_add_f32_e32 v74, 1.0, v74
	v_rcp_f32_e32 v68, v68
	v_rcp_f32_e32 v70, v70
	v_add_f32_e32 v96, 1.0, v96
	v_rcp_f32_e32 v95, v95
	v_mul_f32_e32 v54, v53, v54
	v_pk_fma_f32 v[26:27], v[6:7], v[52:53], v[26:27] op_sel_hi:[1,0,1]
	v_pk_fma_f32 v[16:17], v[8:9], v[52:53], v[16:17] op_sel_hi:[1,0,1]
	v_mul_f32_e32 v52, v83, v91
	v_add_f32_e32 v76, 1.0, v76
	v_add_f32_e32 v78, 1.0, v78
	v_rcp_f32_e32 v72, v72
	v_rcp_f32_e32 v74, v74
	v_add_f32_e32 v97, 1.0, v97
	v_rcp_f32_e32 v96, v96
	v_mul_f32_e32 v56, v55, v56
	v_mul_f32_e32 v58, v57, v58
	v_pk_fma_f32 v[24:25], v[6:7], v[54:55], v[24:25] op_sel_hi:[1,0,1]
	v_pk_fma_f32 v[14:15], v[8:9], v[54:55], v[14:15] op_sel_hi:[1,0,1]
	v_mul_f32_e32 v54, v84, v92
	v_pk_fma_f32 v[8:9], v[8:9], v[52:53], v[12:13] op_sel_hi:[1,0,1]
	v_pk_fma_f32 v[6:7], v[6:7], v[52:53], v[22:23] op_sel_hi:[1,0,1]
	v_add_f32_e32 v80, 1.0, v80
	v_add_f32_e32 v82, 1.0, v82
	v_rcp_f32_e32 v76, v76
	v_rcp_f32_e32 v78, v78
	v_add_f32_e32 v98, 1.0, v98
	v_rcp_f32_e32 v97, v97
	v_mul_f32_e32 v60, v59, v60
	v_mul_f32_e32 v62, v61, v62
	s_waitcnt vmcnt(37)
	v_pk_fma_f32 v[16:17], v[30:31], v[56:57], v[16:17] op_sel_hi:[1,0,1]
	v_pk_fma_f32 v[26:27], v[28:29], v[56:57], v[26:27] op_sel_hi:[1,0,1]
	v_pk_fma_f32 v[14:15], v[30:31], v[58:59], v[14:15] op_sel_hi:[1,0,1]
	v_pk_fma_f32 v[24:25], v[28:29], v[58:59], v[24:25] op_sel_hi:[1,0,1]
	v_mul_f32_e32 v56, v85, v93
	v_pk_fma_f32 v[8:9], v[30:31], v[54:55], v[8:9] op_sel_hi:[1,0,1]
	v_pk_fma_f32 v[6:7], v[28:29], v[54:55], v[6:7] op_sel_hi:[1,0,1]
	v_rcp_f32_e32 v80, v80
	v_rcp_f32_e32 v82, v82
	v_rcp_f32_e32 v98, v98
	v_mul_f32_e32 v64, v63, v64
	v_mul_f32_e32 v66, v65, v66
	v_mul_f32_e32 v58, v86, v94
	s_waitcnt vmcnt(36)
	v_pk_fma_f32 v[12:13], v[34:35], v[60:61], v[16:17] op_sel_hi:[1,0,1]
	v_pk_fma_f32 v[16:17], v[32:33], v[60:61], v[26:27] op_sel_hi:[1,0,1]
	v_pk_fma_f32 v[14:15], v[34:35], v[62:63], v[14:15] op_sel_hi:[1,0,1]
	v_pk_fma_f32 v[22:23], v[32:33], v[62:63], v[24:25] op_sel_hi:[1,0,1]
	v_pk_fma_f32 v[6:7], v[32:33], v[56:57], v[6:7] op_sel_hi:[1,0,1]
	v_pk_fma_f32 v[8:9], v[34:35], v[56:57], v[8:9] op_sel_hi:[1,0,1]
	v_mul_f32_e32 v68, v67, v68
	v_mul_f32_e32 v70, v69, v70
	v_mul_f32_e32 v84, v87, v95
	s_waitcnt vmcnt(35)
	v_pk_fma_f32 v[12:13], v[38:39], v[64:65], v[12:13] op_sel_hi:[1,0,1]
	v_pk_fma_f32 v[16:17], v[36:37], v[64:65], v[16:17] op_sel_hi:[1,0,1]
	v_pk_fma_f32 v[14:15], v[38:39], v[66:67], v[14:15] op_sel_hi:[1,0,1]
	v_pk_fma_f32 v[22:23], v[36:37], v[66:67], v[22:23] op_sel_hi:[1,0,1]
	v_pk_fma_f32 v[8:9], v[38:39], v[58:59], v[8:9] op_sel_hi:[1,0,1]
	v_pk_fma_f32 v[6:7], v[36:37], v[58:59], v[6:7] op_sel_hi:[1,0,1]
	v_mul_f32_e32 v72, v71, v72
	v_mul_f32_e32 v74, v73, v74
	v_mul_f32_e32 v86, v88, v96
	s_waitcnt vmcnt(34)
	v_pk_fma_f32 v[12:13], v[42:43], v[68:69], v[12:13] op_sel_hi:[1,0,1]
	v_pk_fma_f32 v[16:17], v[40:41], v[68:69], v[16:17] op_sel_hi:[1,0,1]
	v_pk_fma_f32 v[14:15], v[42:43], v[70:71], v[14:15] op_sel_hi:[1,0,1]
	v_pk_fma_f32 v[22:23], v[40:41], v[70:71], v[22:23] op_sel_hi:[1,0,1]
	v_pk_fma_f32 v[6:7], v[40:41], v[84:85], v[6:7] op_sel_hi:[1,0,1]
	v_pk_fma_f32 v[8:9], v[42:43], v[84:85], v[8:9] op_sel_hi:[1,0,1]
	v_mul_f32_e32 v76, v75, v76
	v_mul_f32_e32 v78, v77, v78
	v_mul_f32_e32 v88, v89, v97
	s_waitcnt vmcnt(33)
	v_pk_fma_f32 v[12:13], v[46:47], v[72:73], v[12:13] op_sel_hi:[1,0,1]
	v_pk_fma_f32 v[16:17], v[44:45], v[72:73], v[16:17] op_sel_hi:[1,0,1]
	v_pk_fma_f32 v[14:15], v[46:47], v[74:75], v[14:15] op_sel_hi:[1,0,1]
	v_pk_fma_f32 v[22:23], v[44:45], v[74:75], v[22:23] op_sel_hi:[1,0,1]
	v_pk_fma_f32 v[8:9], v[46:47], v[86:87], v[8:9] op_sel_hi:[1,0,1]
	v_pk_fma_f32 v[6:7], v[44:45], v[86:87], v[6:7] op_sel_hi:[1,0,1]
	v_mul_f32_e32 v80, v79, v80
	v_mul_f32_e32 v82, v81, v82
	v_mul_f32_e32 v90, v90, v98
	s_waitcnt vmcnt(32)
	v_pk_fma_f32 v[12:13], v[50:51], v[76:77], v[12:13] op_sel_hi:[1,0,1]
	v_pk_fma_f32 v[24:25], v[48:49], v[76:77], v[16:17] op_sel_hi:[1,0,1]
	v_pk_fma_f32 v[14:15], v[50:51], v[78:79], v[14:15] op_sel_hi:[1,0,1]
	v_pk_fma_f32 v[22:23], v[48:49], v[78:79], v[22:23] op_sel_hi:[1,0,1]
	v_pk_fma_f32 v[6:7], v[48:49], v[88:89], v[6:7] op_sel_hi:[1,0,1]
	v_pk_fma_f32 v[8:9], v[50:51], v[88:89], v[8:9] op_sel_hi:[1,0,1]
	v_pk_fma_f32 v[16:17], v[4:5], v[80:81], v[12:13] op_sel_hi:[1,0,1]
	v_pk_fma_f32 v[26:27], v[2:3], v[80:81], v[24:25] op_sel_hi:[1,0,1]
	v_pk_fma_f32 v[14:15], v[4:5], v[82:83], v[14:15] op_sel_hi:[1,0,1]
	v_pk_fma_f32 v[24:25], v[2:3], v[82:83], v[22:23] op_sel_hi:[1,0,1]
	v_pk_fma_f32 v[12:13], v[4:5], v[90:91], v[8:9] op_sel_hi:[1,0,1]
	v_pk_fma_f32 v[22:23], v[2:3], v[90:91], v[6:7] op_sel_hi:[1,0,1]
	s_cbranch_scc1 .Lmod_tailb
	v_add_co_u32_e32 v6, vcc, s3, v18
	v_lshl_add_u64 v[28:29], s[14:15], 0, v[20:21]
	s_nop 0
	v_addc_co_u32_e32 v7, vcc, -1, v19, vcc
	v_lshl_add_u64 v[8:9], s[18:19], 0, v[20:21]
	global_load_dwordx4 v[2:5], v[18:19], off nt
	global_load_dword v1, v[28:29], off
	global_load_dword v53, v[8:9], off
	global_load_dword v55, v[28:29], off offset:32
	global_load_dword v57, v[8:9], off offset:32
	global_load_dword v59, v[28:29], off offset:64
	global_load_dword v61, v[8:9], off offset:64
	global_load_dword v63, v[28:29], off offset:96
	global_load_dword v65, v[8:9], off offset:96
	global_load_dword v67, v[28:29], off offset:128
	global_load_dword v69, v[8:9], off offset:128
	global_load_dword v71, v[28:29], off offset:160
	global_load_dword v73, v[8:9], off offset:160
	global_load_dword v75, v[28:29], off offset:192
	global_load_dword v77, v[8:9], off offset:192
	global_load_dword v79, v[28:29], off offset:224
	global_load_dword v81, v[8:9], off offset:224
	v_add_co_u32_e32 v28, vcc, s4, v28
	global_load_dwordx4 v[6:9], v[6:7], off nt
	s_nop 0
	v_addc_co_u32_e32 v29, vcc, 0, v29, vcc
	v_add_co_u32_e32 v30, vcc, s5, v18
	global_load_dword v83, v[28:29], off
	global_load_dword v84, v[28:29], off offset:32
	global_load_dword v85, v[28:29], off offset:64
	global_load_dword v86, v[28:29], off offset:96
	global_load_dword v87, v[28:29], off offset:128
	global_load_dword v88, v[28:29], off offset:160
	global_load_dword v89, v[28:29], off offset:192
	global_load_dword v90, v[28:29], off offset:224
	s_waitcnt lgkmcnt(0)
	v_addc_co_u32_e32 v31, vcc, -1, v19, vcc
	v_add_co_u32_e32 v32, vcc, s8, v18
	s_add_i32 s2, s2, 8
	s_nop 0
	v_addc_co_u32_e32 v33, vcc, -1, v19, vcc
	v_add_co_u32_e32 v36, vcc, s9, v18
	global_load_dwordx4 v[28:31], v[30:31], off nt
	s_nop 0
	global_load_dwordx4 v[32:35], v[32:33], off nt
	v_addc_co_u32_e32 v37, vcc, -1, v19, vcc
	v_add_co_u32_e32 v40, vcc, s10, v18
	s_add_u32 s14, s14, 0x100
	s_nop 0
	v_addc_co_u32_e32 v41, vcc, -1, v19, vcc
	v_add_co_u32_e32 v44, vcc, s11, v18
	global_load_dwordx4 v[36:39], v[36:37], off nt
	s_nop 0
	global_load_dwordx4 v[40:43], v[40:41], off nt
	v_addc_co_u32_e32 v45, vcc, -1, v19, vcc
	v_add_co_u32_e32 v48, vcc, s20, v18
	s_addc_u32 s15, s15, 0
	s_nop 0
	v_addc_co_u32_e32 v49, vcc, -1, v19, vcc
	global_load_dwordx4 v[44:47], v[44:45], off nt
	s_nop 0
	global_load_dwordx4 v[48:51], v[48:49], off nt
	s_add_u32 s18, s18, 0x100
	s_addc_u32 s19, s19, 0
	s_cmpk_gt_u32 s2, 0xf7
	v_lshl_add_u64 v[18:19], v[18:19], 0, s[0:1]
	s_waitcnt vmcnt(62)
	v_mul_f32_e32 v194, 0xbfb8aa3b, v161
	s_waitcnt vmcnt(61)
	v_mul_f32_e32 v196, 0xbfb8aa3b, v195
	v_exp_f32_e32 v194, v194
	s_waitcnt vmcnt(60)
	v_mul_f32_e32 v198, 0xbfb8aa3b, v197
	s_waitcnt vmcnt(59)
	v_mul_f32_e32 v200, 0xbfb8aa3b, v199
	v_exp_f32_e32 v196, v196
	s_waitcnt vmcnt(58)
	v_mul_f32_e32 v202, 0xbfb8aa3b, v201
	s_waitcnt vmcnt(57)
	v_mul_f32_e32 v204, 0xbfb8aa3b, v203
	v_exp_f32_e32 v198, v198
	v_exp_f32_e32 v200, v200
	s_waitcnt vmcnt(56)
	v_mul_f32_e32 v206, 0xbfb8aa3b, v205
	s_waitcnt vmcnt(55)
	v_mul_f32_e32 v208, 0xbfb8aa3b, v207
	v_exp_f32_e32 v202, v202
	v_exp_f32_e32 v204, v204
	s_waitcnt vmcnt(54)
	v_mul_f32_e32 v210, 0xbfb8aa3b, v209
	s_waitcnt vmcnt(53)
	v_mul_f32_e32 v212, 0xbfb8aa3b, v211
	s_waitcnt vmcnt(45)
	v_mul_f32_e32 v233, 0xbfb8aa3b, v225
	s_waitcnt vmcnt(44)
	v_mul_f32_e32 v234, 0xbfb8aa3b, v226
	v_exp_f32_e32 v233, v233
	s_waitcnt vmcnt(43)
	v_mul_f32_e32 v235, 0xbfb8aa3b, v227
	v_exp_f32_e32 v234, v234
	s_waitcnt vmcnt(42)
	v_mul_f32_e32 v236, 0xbfb8aa3b, v228
	v_exp_f32_e32 v235, v235
	v_exp_f32_e32 v206, v206
	v_exp_f32_e32 v208, v208
	s_waitcnt vmcnt(41)
	v_mul_f32_e32 v237, 0xbfb8aa3b, v229
	v_exp_f32_e32 v236, v236
	v_add_f32_e32 v194, 1.0, v194
	v_mul_f32_e32 v214, 0xbfb8aa3b, v213
	v_mul_f32_e32 v216, 0xbfb8aa3b, v215
	v_exp_f32_e32 v210, v210
	v_exp_f32_e32 v212, v212
	s_waitcnt vmcnt(40)
	v_mul_f32_e32 v238, 0xbfb8aa3b, v230
	v_exp_f32_e32 v237, v237
	v_add_f32_e32 v196, 1.0, v196
	v_rcp_f32_e32 v194, v194
	v_add_f32_e32 v233, 1.0, v233
	v_mul_f32_e32 v218, 0xbfb8aa3b, v217
	v_mul_f32_e32 v220, 0xbfb8aa3b, v219
	v_exp_f32_e32 v214, v214
	v_exp_f32_e32 v216, v216
	s_waitcnt vmcnt(39)
	v_mul_f32_e32 v239, 0xbfb8aa3b, v231
	v_exp_f32_e32 v238, v238
	v_add_f32_e32 v198, 1.0, v198
	v_add_f32_e32 v200, 1.0, v200
	v_rcp_f32_e32 v196, v196
	v_add_f32_e32 v234, 1.0, v234
	v_rcp_f32_e32 v233, v233
	v_mul_f32_e32 v222, 0xbfb8aa3b, v221
	v_mul_f32_e32 v224, 0xbfb8aa3b, v223
	v_exp_f32_e32 v218, v218
	v_exp_f32_e32 v220, v220
	s_waitcnt vmcnt(38)
	v_mul_f32_e32 v240, 0xbfb8aa3b, v232
	v_exp_f32_e32 v239, v239
	v_add_f32_e32 v202, 1.0, v202
	v_add_f32_e32 v204, 1.0, v204
	v_rcp_f32_e32 v198, v198
	v_rcp_f32_e32 v200, v200
	v_add_f32_e32 v235, 1.0, v235
	v_rcp_f32_e32 v234, v234
	v_exp_f32_e32 v222, v222
	v_exp_f32_e32 v224, v224
	v_exp_f32_e32 v240, v240
	v_add_f32_e32 v206, 1.0, v206
	v_add_f32_e32 v208, 1.0, v208
	v_rcp_f32_e32 v202, v202
	v_rcp_f32_e32 v204, v204
	v_add_f32_e32 v236, 1.0, v236
	v_rcp_f32_e32 v235, v235
	v_add_f32_e32 v210, 1.0, v210
	v_add_f32_e32 v212, 1.0, v212
	v_rcp_f32_e32 v206, v206
	v_rcp_f32_e32 v208, v208
	v_add_f32_e32 v237, 1.0, v237
	v_rcp_f32_e32 v236, v236
	v_mul_f32_e32 v194, v161, v194
	v_add_f32_e32 v214, 1.0, v214
	v_add_f32_e32 v216, 1.0, v216
	v_rcp_f32_e32 v210, v210
	v_rcp_f32_e32 v212, v212
	v_add_f32_e32 v238, 1.0, v238
	v_rcp_f32_e32 v237, v237
	v_mul_f32_e32 v196, v195, v196
	v_pk_fma_f32 v[26:27], v[166:167], v[194:195], v[26:27] op_sel_hi:[1,0,1]
	v_pk_fma_f32 v[16:17], v[168:169], v[194:195], v[16:17] op_sel_hi:[1,0,1]
	v_mul_f32_e32 v194, v225, v233
	v_add_f32_e32 v218, 1.0, v218
	v_add_f32_e32 v220, 1.0, v220
	v_rcp_f32_e32 v214, v214
	v_rcp_f32_e32 v216, v216
	v_add_f32_e32 v239, 1.0, v239
	v_rcp_f32_e32 v238, v238
	v_mul_f32_e32 v198, v197, v198
	v_mul_f32_e32 v200, v199, v200
	v_pk_fma_f32 v[24:25], v[166:167], v[196:197], v[24:25] op_sel_hi:[1,0,1]
	v_pk_fma_f32 v[14:15], v[168:169], v[196:197], v[14:15] op_sel_hi:[1,0,1]
	v_mul_f32_e32 v196, v226, v234
	v_pk_fma_f32 v[168:169], v[168:169], v[194:195], v[12:13] op_sel_hi:[1,0,1]
	v_pk_fma_f32 v[166:167], v[166:167], v[194:195], v[22:23] op_sel_hi:[1,0,1]
	v_add_f32_e32 v222, 1.0, v222
	v_add_f32_e32 v224, 1.0, v224
	v_rcp_f32_e32 v218, v218
	v_rcp_f32_e32 v220, v220
	v_add_f32_e32 v240, 1.0, v240
	v_rcp_f32_e32 v239, v239
	v_mul_f32_e32 v202, v201, v202
	v_mul_f32_e32 v204, v203, v204
	s_waitcnt vmcnt(37)
	v_pk_fma_f32 v[16:17], v[172:173], v[198:199], v[16:17] op_sel_hi:[1,0,1]
	v_pk_fma_f32 v[26:27], v[170:171], v[198:199], v[26:27] op_sel_hi:[1,0,1]
	v_pk_fma_f32 v[14:15], v[172:173], v[200:201], v[14:15] op_sel_hi:[1,0,1]
	v_pk_fma_f32 v[24:25], v[170:171], v[200:201], v[24:25] op_sel_hi:[1,0,1]
	v_mul_f32_e32 v198, v227, v235
	v_pk_fma_f32 v[168:169], v[172:173], v[196:197], v[168:169] op_sel_hi:[1,0,1]
	v_pk_fma_f32 v[166:167], v[170:171], v[196:197], v[166:167] op_sel_hi:[1,0,1]
	v_rcp_f32_e32 v222, v222
	v_rcp_f32_e32 v224, v224
	v_rcp_f32_e32 v240, v240
	v_mul_f32_e32 v206, v205, v206
	v_mul_f32_e32 v208, v207, v208
	v_mul_f32_e32 v200, v228, v236
	s_waitcnt vmcnt(36)
	v_pk_fma_f32 v[12:13], v[176:177], v[202:203], v[16:17] op_sel_hi:[1,0,1]
	v_pk_fma_f32 v[16:17], v[174:175], v[202:203], v[26:27] op_sel_hi:[1,0,1]
	v_pk_fma_f32 v[14:15], v[176:177], v[204:205], v[14:15] op_sel_hi:[1,0,1]
	v_pk_fma_f32 v[22:23], v[174:175], v[204:205], v[24:25] op_sel_hi:[1,0,1]
	v_pk_fma_f32 v[166:167], v[174:175], v[198:199], v[166:167] op_sel_hi:[1,0,1]
	v_pk_fma_f32 v[168:169], v[176:177], v[198:199], v[168:169] op_sel_hi:[1,0,1]
	v_mul_f32_e32 v210, v209, v210
	v_mul_f32_e32 v212, v211, v212
	v_mul_f32_e32 v226, v229, v237
	s_waitcnt vmcnt(35)
	v_pk_fma_f32 v[12:13], v[180:181], v[206:207], v[12:13] op_sel_hi:[1,0,1]
	v_pk_fma_f32 v[16:17], v[178:179], v[206:207], v[16:17] op_sel_hi:[1,0,1]
	v_pk_fma_f32 v[14:15], v[180:181], v[208:209], v[14:15] op_sel_hi:[1,0,1]
	v_pk_fma_f32 v[22:23], v[178:179], v[208:209], v[22:23] op_sel_hi:[1,0,1]
	v_pk_fma_f32 v[168:169], v[180:181], v[200:201], v[168:169] op_sel_hi:[1,0,1]
	v_pk_fma_f32 v[166:167], v[178:179], v[200:201], v[166:167] op_sel_hi:[1,0,1]
	v_mul_f32_e32 v214, v213, v214
	v_mul_f32_e32 v216, v215, v216
	v_mul_f32_e32 v228, v230, v238
	s_waitcnt vmcnt(34)
	v_pk_fma_f32 v[12:13], v[184:185], v[210:211], v[12:13] op_sel_hi:[1,0,1]
	v_pk_fma_f32 v[16:17], v[182:183], v[210:211], v[16:17] op_sel_hi:[1,0,1]
	v_pk_fma_f32 v[14:15], v[184:185], v[212:213], v[14:15] op_sel_hi:[1,0,1]
	v_pk_fma_f32 v[22:23], v[182:183], v[212:213], v[22:23] op_sel_hi:[1,0,1]
	v_pk_fma_f32 v[166:167], v[182:183], v[226:227], v[166:167] op_sel_hi:[1,0,1]
	v_pk_fma_f32 v[168:169], v[184:185], v[226:227], v[168:169] op_sel_hi:[1,0,1]
	v_mul_f32_e32 v218, v217, v218
	v_mul_f32_e32 v220, v219, v220
	v_mul_f32_e32 v230, v231, v239
	s_waitcnt vmcnt(33)
	v_pk_fma_f32 v[12:13], v[188:189], v[214:215], v[12:13] op_sel_hi:[1,0,1]
	v_pk_fma_f32 v[16:17], v[186:187], v[214:215], v[16:17] op_sel_hi:[1,0,1]
	v_pk_fma_f32 v[14:15], v[188:189], v[216:217], v[14:15] op_sel_hi:[1,0,1]
	v_pk_fma_f32 v[22:23], v[186:187], v[216:217], v[22:23] op_sel_hi:[1,0,1]
	v_pk_fma_f32 v[168:169], v[188:189], v[228:229], v[168:169] op_sel_hi:[1,0,1]
	v_pk_fma_f32 v[166:167], v[186:187], v[228:229], v[166:167] op_sel_hi:[1,0,1]
	v_mul_f32_e32 v222, v221, v222
	v_mul_f32_e32 v224, v223, v224
	v_mul_f32_e32 v232, v232, v240
	s_waitcnt vmcnt(32)
	v_pk_fma_f32 v[12:13], v[192:193], v[218:219], v[12:13] op_sel_hi:[1,0,1]
	v_pk_fma_f32 v[24:25], v[190:191], v[218:219], v[16:17] op_sel_hi:[1,0,1]
	v_pk_fma_f32 v[14:15], v[192:193], v[220:221], v[14:15] op_sel_hi:[1,0,1]
	v_pk_fma_f32 v[22:23], v[190:191], v[220:221], v[22:23] op_sel_hi:[1,0,1]
	v_pk_fma_f32 v[166:167], v[190:191], v[230:231], v[166:167] op_sel_hi:[1,0,1]
	v_pk_fma_f32 v[168:169], v[192:193], v[230:231], v[168:169] op_sel_hi:[1,0,1]
	v_pk_fma_f32 v[16:17], v[164:165], v[222:223], v[12:13] op_sel_hi:[1,0,1]
	v_pk_fma_f32 v[26:27], v[162:163], v[222:223], v[24:25] op_sel_hi:[1,0,1]
	v_pk_fma_f32 v[14:15], v[164:165], v[224:225], v[14:15] op_sel_hi:[1,0,1]
	v_pk_fma_f32 v[24:25], v[162:163], v[224:225], v[22:23] op_sel_hi:[1,0,1]
	v_pk_fma_f32 v[12:13], v[164:165], v[232:233], v[168:169] op_sel_hi:[1,0,1]
	v_pk_fma_f32 v[22:23], v[162:163], v[232:233], v[166:167] op_sel_hi:[1,0,1]
	s_cbranch_scc0 .Lmod_loop
	s_waitcnt vmcnt(30)
	v_mul_f32_e32 v52, 0xbfb8aa3b, v1
	s_waitcnt vmcnt(29)
	v_mul_f32_e32 v54, 0xbfb8aa3b, v53
	v_exp_f32_e32 v52, v52
	s_waitcnt vmcnt(28)
	v_mul_f32_e32 v56, 0xbfb8aa3b, v55
	s_waitcnt vmcnt(27)
	v_mul_f32_e32 v58, 0xbfb8aa3b, v57
	v_exp_f32_e32 v54, v54
	s_waitcnt vmcnt(26)
	v_mul_f32_e32 v60, 0xbfb8aa3b, v59
	s_waitcnt vmcnt(25)
	v_mul_f32_e32 v62, 0xbfb8aa3b, v61
	v_exp_f32_e32 v56, v56
	v_exp_f32_e32 v58, v58
	s_waitcnt vmcnt(24)
	v_mul_f32_e32 v64, 0xbfb8aa3b, v63
	s_waitcnt vmcnt(23)
	v_mul_f32_e32 v66, 0xbfb8aa3b, v65
	v_exp_f32_e32 v60, v60
	v_exp_f32_e32 v62, v62
	s_waitcnt vmcnt(22)
	v_mul_f32_e32 v68, 0xbfb8aa3b, v67
	s_waitcnt vmcnt(21)
	v_mul_f32_e32 v70, 0xbfb8aa3b, v69
	s_waitcnt vmcnt(13)
	v_mul_f32_e32 v91, 0xbfb8aa3b, v83
	s_waitcnt vmcnt(12)
	v_mul_f32_e32 v92, 0xbfb8aa3b, v84
	v_exp_f32_e32 v91, v91
	s_waitcnt vmcnt(11)
	v_mul_f32_e32 v93, 0xbfb8aa3b, v85
	v_exp_f32_e32 v92, v92
	s_waitcnt vmcnt(10)
	v_mul_f32_e32 v94, 0xbfb8aa3b, v86
	v_exp_f32_e32 v93, v93
	v_exp_f32_e32 v64, v64
	v_exp_f32_e32 v66, v66
	s_waitcnt vmcnt(9)
	v_mul_f32_e32 v95, 0xbfb8aa3b, v87
	v_exp_f32_e32 v94, v94
	v_add_f32_e32 v52, 1.0, v52
	v_mul_f32_e32 v72, 0xbfb8aa3b, v71
	v_mul_f32_e32 v74, 0xbfb8aa3b, v73
	v_exp_f32_e32 v68, v68
	v_exp_f32_e32 v70, v70
	s_waitcnt vmcnt(8)
	v_mul_f32_e32 v96, 0xbfb8aa3b, v88
	v_exp_f32_e32 v95, v95
	v_add_f32_e32 v54, 1.0, v54
	v_rcp_f32_e32 v52, v52
	v_add_f32_e32 v91, 1.0, v91
	v_mul_f32_e32 v76, 0xbfb8aa3b, v75
	v_mul_f32_e32 v78, 0xbfb8aa3b, v77
	v_exp_f32_e32 v72, v72
	v_exp_f32_e32 v74, v74
	s_waitcnt vmcnt(7)
	v_mul_f32_e32 v97, 0xbfb8aa3b, v89
	v_exp_f32_e32 v96, v96
	v_add_f32_e32 v56, 1.0, v56
	v_add_f32_e32 v58, 1.0, v58
	v_rcp_f32_e32 v54, v54
	v_add_f32_e32 v92, 1.0, v92
	v_rcp_f32_e32 v91, v91
	v_mul_f32_e32 v80, 0xbfb8aa3b, v79
	v_mul_f32_e32 v82, 0xbfb8aa3b, v81
	v_exp_f32_e32 v76, v76
	v_exp_f32_e32 v78, v78
	s_waitcnt vmcnt(6)
	v_mul_f32_e32 v98, 0xbfb8aa3b, v90
	v_exp_f32_e32 v97, v97
	v_add_f32_e32 v60, 1.0, v60
	v_add_f32_e32 v62, 1.0, v62
	v_rcp_f32_e32 v56, v56
	v_rcp_f32_e32 v58, v58
	v_add_f32_e32 v93, 1.0, v93
	v_rcp_f32_e32 v92, v92
	v_exp_f32_e32 v80, v80
	v_exp_f32_e32 v82, v82
	v_exp_f32_e32 v98, v98
	v_add_f32_e32 v64, 1.0, v64
	v_add_f32_e32 v66, 1.0, v66
	v_rcp_f32_e32 v60, v60
	v_rcp_f32_e32 v62, v62
	v_add_f32_e32 v94, 1.0, v94
	v_rcp_f32_e32 v93, v93
	v_add_f32_e32 v68, 1.0, v68
	v_add_f32_e32 v70, 1.0, v70
	v_rcp_f32_e32 v64, v64
	v_rcp_f32_e32 v66, v66
	v_add_f32_e32 v95, 1.0, v95
	v_rcp_f32_e32 v94, v94
	v_mul_f32_e32 v52, v1, v52
	v_add_f32_e32 v72, 1.0, v72
	v_add_f32_e32 v74, 1.0, v74
	v_rcp_f32_e32 v68, v68
	v_rcp_f32_e32 v70, v70
	v_add_f32_e32 v96, 1.0, v96
	v_rcp_f32_e32 v95, v95
	v_mul_f32_e32 v54, v53, v54
	v_pk_fma_f32 v[26:27], v[6:7], v[52:53], v[26:27] op_sel_hi:[1,0,1]
	v_pk_fma_f32 v[16:17], v[8:9], v[52:53], v[16:17] op_sel_hi:[1,0,1]
	v_mul_f32_e32 v52, v83, v91
	v_add_f32_e32 v76, 1.0, v76
	v_add_f32_e32 v78, 1.0, v78
	v_rcp_f32_e32 v72, v72
	v_rcp_f32_e32 v74, v74
	v_add_f32_e32 v97, 1.0, v97
	v_rcp_f32_e32 v96, v96
	v_mul_f32_e32 v56, v55, v56
	v_mul_f32_e32 v58, v57, v58
	v_pk_fma_f32 v[24:25], v[6:7], v[54:55], v[24:25] op_sel_hi:[1,0,1]
	v_pk_fma_f32 v[14:15], v[8:9], v[54:55], v[14:15] op_sel_hi:[1,0,1]
	v_mul_f32_e32 v54, v84, v92
	v_pk_fma_f32 v[8:9], v[8:9], v[52:53], v[12:13] op_sel_hi:[1,0,1]
	v_pk_fma_f32 v[6:7], v[6:7], v[52:53], v[22:23] op_sel_hi:[1,0,1]
	v_add_f32_e32 v80, 1.0, v80
	v_add_f32_e32 v82, 1.0, v82
	v_rcp_f32_e32 v76, v76
	v_rcp_f32_e32 v78, v78
	v_add_f32_e32 v98, 1.0, v98
	v_rcp_f32_e32 v97, v97
	v_mul_f32_e32 v60, v59, v60
	v_mul_f32_e32 v62, v61, v62
	s_waitcnt vmcnt(5)
	v_pk_fma_f32 v[16:17], v[30:31], v[56:57], v[16:17] op_sel_hi:[1,0,1]
	v_pk_fma_f32 v[26:27], v[28:29], v[56:57], v[26:27] op_sel_hi:[1,0,1]
	v_pk_fma_f32 v[14:15], v[30:31], v[58:59], v[14:15] op_sel_hi:[1,0,1]
	v_pk_fma_f32 v[24:25], v[28:29], v[58:59], v[24:25] op_sel_hi:[1,0,1]
	v_mul_f32_e32 v56, v85, v93
	v_pk_fma_f32 v[8:9], v[30:31], v[54:55], v[8:9] op_sel_hi:[1,0,1]
	v_pk_fma_f32 v[6:7], v[28:29], v[54:55], v[6:7] op_sel_hi:[1,0,1]
	v_rcp_f32_e32 v80, v80
	v_rcp_f32_e32 v82, v82
	v_rcp_f32_e32 v98, v98
	v_mul_f32_e32 v64, v63, v64
	v_mul_f32_e32 v66, v65, v66
	v_mul_f32_e32 v58, v86, v94
	s_waitcnt vmcnt(4)
	v_pk_fma_f32 v[12:13], v[34:35], v[60:61], v[16:17] op_sel_hi:[1,0,1]
	v_pk_fma_f32 v[16:17], v[32:33], v[60:61], v[26:27] op_sel_hi:[1,0,1]
	v_pk_fma_f32 v[14:15], v[34:35], v[62:63], v[14:15] op_sel_hi:[1,0,1]
	v_pk_fma_f32 v[22:23], v[32:33], v[62:63], v[24:25] op_sel_hi:[1,0,1]
	v_pk_fma_f32 v[6:7], v[32:33], v[56:57], v[6:7] op_sel_hi:[1,0,1]
	v_pk_fma_f32 v[8:9], v[34:35], v[56:57], v[8:9] op_sel_hi:[1,0,1]
	v_mul_f32_e32 v68, v67, v68
	v_mul_f32_e32 v70, v69, v70
	v_mul_f32_e32 v84, v87, v95
	s_waitcnt vmcnt(3)
	v_pk_fma_f32 v[12:13], v[38:39], v[64:65], v[12:13] op_sel_hi:[1,0,1]
	v_pk_fma_f32 v[16:17], v[36:37], v[64:65], v[16:17] op_sel_hi:[1,0,1]
	v_pk_fma_f32 v[14:15], v[38:39], v[66:67], v[14:15] op_sel_hi:[1,0,1]
	v_pk_fma_f32 v[22:23], v[36:37], v[66:67], v[22:23] op_sel_hi:[1,0,1]
	v_pk_fma_f32 v[8:9], v[38:39], v[58:59], v[8:9] op_sel_hi:[1,0,1]
	v_pk_fma_f32 v[6:7], v[36:37], v[58:59], v[6:7] op_sel_hi:[1,0,1]
	v_mul_f32_e32 v72, v71, v72
	v_mul_f32_e32 v74, v73, v74
	v_mul_f32_e32 v86, v88, v96
	s_waitcnt vmcnt(2)
	v_pk_fma_f32 v[12:13], v[42:43], v[68:69], v[12:13] op_sel_hi:[1,0,1]
	v_pk_fma_f32 v[16:17], v[40:41], v[68:69], v[16:17] op_sel_hi:[1,0,1]
	v_pk_fma_f32 v[14:15], v[42:43], v[70:71], v[14:15] op_sel_hi:[1,0,1]
	v_pk_fma_f32 v[22:23], v[40:41], v[70:71], v[22:23] op_sel_hi:[1,0,1]
	v_pk_fma_f32 v[6:7], v[40:41], v[84:85], v[6:7] op_sel_hi:[1,0,1]
	v_pk_fma_f32 v[8:9], v[42:43], v[84:85], v[8:9] op_sel_hi:[1,0,1]
	v_mul_f32_e32 v76, v75, v76
	v_mul_f32_e32 v78, v77, v78
	v_mul_f32_e32 v88, v89, v97
	s_waitcnt vmcnt(1)
	v_pk_fma_f32 v[12:13], v[46:47], v[72:73], v[12:13] op_sel_hi:[1,0,1]
	v_pk_fma_f32 v[16:17], v[44:45], v[72:73], v[16:17] op_sel_hi:[1,0,1]
	v_pk_fma_f32 v[14:15], v[46:47], v[74:75], v[14:15] op_sel_hi:[1,0,1]
	v_pk_fma_f32 v[22:23], v[44:45], v[74:75], v[22:23] op_sel_hi:[1,0,1]
	v_pk_fma_f32 v[8:9], v[46:47], v[86:87], v[8:9] op_sel_hi:[1,0,1]
	v_pk_fma_f32 v[6:7], v[44:45], v[86:87], v[6:7] op_sel_hi:[1,0,1]
	v_mul_f32_e32 v80, v79, v80
	v_mul_f32_e32 v82, v81, v82
	v_mul_f32_e32 v90, v90, v98
	s_waitcnt vmcnt(0)
	v_pk_fma_f32 v[12:13], v[50:51], v[76:77], v[12:13] op_sel_hi:[1,0,1]
	v_pk_fma_f32 v[24:25], v[48:49], v[76:77], v[16:17] op_sel_hi:[1,0,1]
	v_pk_fma_f32 v[14:15], v[50:51], v[78:79], v[14:15] op_sel_hi:[1,0,1]
	v_pk_fma_f32 v[22:23], v[48:49], v[78:79], v[22:23] op_sel_hi:[1,0,1]
	v_pk_fma_f32 v[6:7], v[48:49], v[88:89], v[6:7] op_sel_hi:[1,0,1]
	v_pk_fma_f32 v[8:9], v[50:51], v[88:89], v[8:9] op_sel_hi:[1,0,1]
	v_pk_fma_f32 v[16:17], v[4:5], v[80:81], v[12:13] op_sel_hi:[1,0,1]
	v_pk_fma_f32 v[26:27], v[2:3], v[80:81], v[24:25] op_sel_hi:[1,0,1]
	v_pk_fma_f32 v[14:15], v[4:5], v[82:83], v[14:15] op_sel_hi:[1,0,1]
	v_pk_fma_f32 v[24:25], v[2:3], v[82:83], v[22:23] op_sel_hi:[1,0,1]
	v_pk_fma_f32 v[12:13], v[4:5], v[90:91], v[8:9] op_sel_hi:[1,0,1]
	v_pk_fma_f32 v[22:23], v[2:3], v[90:91], v[6:7] op_sel_hi:[1,0,1]
	s_branch .Lmod_done
.Lmod_tailb:
	s_waitcnt vmcnt(30)
	v_mul_f32_e32 v194, 0xbfb8aa3b, v161
	s_waitcnt vmcnt(29)
	v_mul_f32_e32 v196, 0xbfb8aa3b, v195
	v_exp_f32_e32 v194, v194
	s_waitcnt vmcnt(28)
	v_mul_f32_e32 v198, 0xbfb8aa3b, v197
	s_waitcnt vmcnt(27)
	v_mul_f32_e32 v200, 0xbfb8aa3b, v199
	v_exp_f32_e32 v196, v196
	s_waitcnt vmcnt(26)
	v_mul_f32_e32 v202, 0xbfb8aa3b, v201
	s_waitcnt vmcnt(25)
	v_mul_f32_e32 v204, 0xbfb8aa3b, v203
	v_exp_f32_e32 v198, v198
	v_exp_f32_e32 v200, v200
	s_waitcnt vmcnt(24)
	v_mul_f32_e32 v206, 0xbfb8aa3b, v205
	s_waitcnt vmcnt(23)
	v_mul_f32_e32 v208, 0xbfb8aa3b, v207
	v_exp_f32_e32 v202, v202
	v_exp_f32_e32 v204, v204
	s_waitcnt vmcnt(22)
	v_mul_f32_e32 v210, 0xbfb8aa3b, v209
	s_waitcnt vmcnt(21)
	v_mul_f32_e32 v212, 0xbfb8aa3b, v211
	s_waitcnt vmcnt(13)
	v_mul_f32_e32 v233, 0xbfb8aa3b, v225
	s_waitcnt vmcnt(12)
	v_mul_f32_e32 v234, 0xbfb8aa3b, v226
	v_exp_f32_e32 v233, v233
	s_waitcnt vmcnt(11)
	v_mul_f32_e32 v235, 0xbfb8aa3b, v227
	v_exp_f32_e32 v234, v234
	s_waitcnt vmcnt(10)
	v_mul_f32_e32 v236, 0xbfb8aa3b, v228
	v_exp_f32_e32 v235, v235
	v_exp_f32_e32 v206, v206
	v_exp_f32_e32 v208, v208
	s_waitcnt vmcnt(9)
	v_mul_f32_e32 v237, 0xbfb8aa3b, v229
	v_exp_f32_e32 v236, v236
	v_add_f32_e32 v194, 1.0, v194
	v_mul_f32_e32 v214, 0xbfb8aa3b, v213
	v_mul_f32_e32 v216, 0xbfb8aa3b, v215
	v_exp_f32_e32 v210, v210
	v_exp_f32_e32 v212, v212
	s_waitcnt vmcnt(8)
	v_mul_f32_e32 v238, 0xbfb8aa3b, v230
	v_exp_f32_e32 v237, v237
	v_add_f32_e32 v196, 1.0, v196
	v_rcp_f32_e32 v194, v194
	v_add_f32_e32 v233, 1.0, v233
	v_mul_f32_e32 v218, 0xbfb8aa3b, v217
	v_mul_f32_e32 v220, 0xbfb8aa3b, v219
	v_exp_f32_e32 v214, v214
	v_exp_f32_e32 v216, v216
	s_waitcnt vmcnt(7)
	v_mul_f32_e32 v239, 0xbfb8aa3b, v231
	v_exp_f32_e32 v238, v238
	v_add_f32_e32 v198, 1.0, v198
	v_add_f32_e32 v200, 1.0, v200
	v_rcp_f32_e32 v196, v196
	v_add_f32_e32 v234, 1.0, v234
	v_rcp_f32_e32 v233, v233
	v_mul_f32_e32 v222, 0xbfb8aa3b, v221
	v_mul_f32_e32 v224, 0xbfb8aa3b, v223
	v_exp_f32_e32 v218, v218
	v_exp_f32_e32 v220, v220
	s_waitcnt vmcnt(6)
	v_mul_f32_e32 v240, 0xbfb8aa3b, v232
	v_exp_f32_e32 v239, v239
	v_add_f32_e32 v202, 1.0, v202
	v_add_f32_e32 v204, 1.0, v204
	v_rcp_f32_e32 v198, v198
	v_rcp_f32_e32 v200, v200
	v_add_f32_e32 v235, 1.0, v235
	v_rcp_f32_e32 v234, v234
	v_exp_f32_e32 v222, v222
	v_exp_f32_e32 v224, v224
	v_exp_f32_e32 v240, v240
	v_add_f32_e32 v206, 1.0, v206
	v_add_f32_e32 v208, 1.0, v208
	v_rcp_f32_e32 v202, v202
	v_rcp_f32_e32 v204, v204
	v_add_f32_e32 v236, 1.0, v236
	v_rcp_f32_e32 v235, v235
	v_add_f32_e32 v210, 1.0, v210
	v_add_f32_e32 v212, 1.0, v212
	v_rcp_f32_e32 v206, v206
	v_rcp_f32_e32 v208, v208
	v_add_f32_e32 v237, 1.0, v237
	v_rcp_f32_e32 v236, v236
	v_mul_f32_e32 v194, v161, v194
	v_add_f32_e32 v214, 1.0, v214
	v_add_f32_e32 v216, 1.0, v216
	v_rcp_f32_e32 v210, v210
	v_rcp_f32_e32 v212, v212
	v_add_f32_e32 v238, 1.0, v238
	v_rcp_f32_e32 v237, v237
	v_mul_f32_e32 v196, v195, v196
	v_pk_fma_f32 v[26:27], v[166:167], v[194:195], v[26:27] op_sel_hi:[1,0,1]
	v_pk_fma_f32 v[16:17], v[168:169], v[194:195], v[16:17] op_sel_hi:[1,0,1]
	v_mul_f32_e32 v194, v225, v233
	v_add_f32_e32 v218, 1.0, v218
	v_add_f32_e32 v220, 1.0, v220
	v_rcp_f32_e32 v214, v214
	v_rcp_f32_e32 v216, v216
	v_add_f32_e32 v239, 1.0, v239
	v_rcp_f32_e32 v238, v238
	v_mul_f32_e32 v198, v197, v198
	v_mul_f32_e32 v200, v199, v200
	v_pk_fma_f32 v[24:25], v[166:167], v[196:197], v[24:25] op_sel_hi:[1,0,1]
	v_pk_fma_f32 v[14:15], v[168:169], v[196:197], v[14:15] op_sel_hi:[1,0,1]
	v_mul_f32_e32 v196, v226, v234
	v_pk_fma_f32 v[168:169], v[168:169], v[194:195], v[12:13] op_sel_hi:[1,0,1]
	v_pk_fma_f32 v[166:167], v[166:167], v[194:195], v[22:23] op_sel_hi:[1,0,1]
	v_add_f32_e32 v222, 1.0, v222
	v_add_f32_e32 v224, 1.0, v224
	v_rcp_f32_e32 v218, v218
	v_rcp_f32_e32 v220, v220
	v_add_f32_e32 v240, 1.0, v240
	v_rcp_f32_e32 v239, v239
	v_mul_f32_e32 v202, v201, v202
	v_mul_f32_e32 v204, v203, v204
	s_waitcnt vmcnt(5)
	v_pk_fma_f32 v[16:17], v[172:173], v[198:199], v[16:17] op_sel_hi:[1,0,1]
	v_pk_fma_f32 v[26:27], v[170:171], v[198:199], v[26:27] op_sel_hi:[1,0,1]
	v_pk_fma_f32 v[14:15], v[172:173], v[200:201], v[14:15] op_sel_hi:[1,0,1]
	v_pk_fma_f32 v[24:25], v[170:171], v[200:201], v[24:25] op_sel_hi:[1,0,1]
	v_mul_f32_e32 v198, v227, v235
	v_pk_fma_f32 v[168:169], v[172:173], v[196:197], v[168:169] op_sel_hi:[1,0,1]
	v_pk_fma_f32 v[166:167], v[170:171], v[196:197], v[166:167] op_sel_hi:[1,0,1]
	v_rcp_f32_e32 v222, v222
	v_rcp_f32_e32 v224, v224
	v_rcp_f32_e32 v240, v240
	v_mul_f32_e32 v206, v205, v206
	v_mul_f32_e32 v208, v207, v208
	v_mul_f32_e32 v200, v228, v236
	s_waitcnt vmcnt(4)
	v_pk_fma_f32 v[12:13], v[176:177], v[202:203], v[16:17] op_sel_hi:[1,0,1]
	v_pk_fma_f32 v[16:17], v[174:175], v[202:203], v[26:27] op_sel_hi:[1,0,1]
	v_pk_fma_f32 v[14:15], v[176:177], v[204:205], v[14:15] op_sel_hi:[1,0,1]
	v_pk_fma_f32 v[22:23], v[174:175], v[204:205], v[24:25] op_sel_hi:[1,0,1]
	v_pk_fma_f32 v[166:167], v[174:175], v[198:199], v[166:167] op_sel_hi:[1,0,1]
	v_pk_fma_f32 v[168:169], v[176:177], v[198:199], v[168:169] op_sel_hi:[1,0,1]
	v_mul_f32_e32 v210, v209, v210
	v_mul_f32_e32 v212, v211, v212
	v_mul_f32_e32 v226, v229, v237
	s_waitcnt vmcnt(3)
	v_pk_fma_f32 v[12:13], v[180:181], v[206:207], v[12:13] op_sel_hi:[1,0,1]
	v_pk_fma_f32 v[16:17], v[178:179], v[206:207], v[16:17] op_sel_hi:[1,0,1]
	v_pk_fma_f32 v[14:15], v[180:181], v[208:209], v[14:15] op_sel_hi:[1,0,1]
	v_pk_fma_f32 v[22:23], v[178:179], v[208:209], v[22:23] op_sel_hi:[1,0,1]
	v_pk_fma_f32 v[168:169], v[180:181], v[200:201], v[168:169] op_sel_hi:[1,0,1]
	v_pk_fma_f32 v[166:167], v[178:179], v[200:201], v[166:167] op_sel_hi:[1,0,1]
	v_mul_f32_e32 v214, v213, v214
	v_mul_f32_e32 v216, v215, v216
	v_mul_f32_e32 v228, v230, v238
	s_waitcnt vmcnt(2)
	v_pk_fma_f32 v[12:13], v[184:185], v[210:211], v[12:13] op_sel_hi:[1,0,1]
	v_pk_fma_f32 v[16:17], v[182:183], v[210:211], v[16:17] op_sel_hi:[1,0,1]
	v_pk_fma_f32 v[14:15], v[184:185], v[212:213], v[14:15] op_sel_hi:[1,0,1]
	v_pk_fma_f32 v[22:23], v[182:183], v[212:213], v[22:23] op_sel_hi:[1,0,1]
	v_pk_fma_f32 v[166:167], v[182:183], v[226:227], v[166:167] op_sel_hi:[1,0,1]
	v_pk_fma_f32 v[168:169], v[184:185], v[226:227], v[168:169] op_sel_hi:[1,0,1]
	v_mul_f32_e32 v218, v217, v218
	v_mul_f32_e32 v220, v219, v220
	v_mul_f32_e32 v230, v231, v239
	s_waitcnt vmcnt(1)
	v_pk_fma_f32 v[12:13], v[188:189], v[214:215], v[12:13] op_sel_hi:[1,0,1]
	v_pk_fma_f32 v[16:17], v[186:187], v[214:215], v[16:17] op_sel_hi:[1,0,1]
	v_pk_fma_f32 v[14:15], v[188:189], v[216:217], v[14:15] op_sel_hi:[1,0,1]
	v_pk_fma_f32 v[22:23], v[186:187], v[216:217], v[22:23] op_sel_hi:[1,0,1]
	v_pk_fma_f32 v[168:169], v[188:189], v[228:229], v[168:169] op_sel_hi:[1,0,1]
	v_pk_fma_f32 v[166:167], v[186:187], v[228:229], v[166:167] op_sel_hi:[1,0,1]
	v_mul_f32_e32 v222, v221, v222
	v_mul_f32_e32 v224, v223, v224
	v_mul_f32_e32 v232, v232, v240
	s_waitcnt vmcnt(0)
	v_pk_fma_f32 v[12:13], v[192:193], v[218:219], v[12:13] op_sel_hi:[1,0,1]
	v_pk_fma_f32 v[24:25], v[190:191], v[218:219], v[16:17] op_sel_hi:[1,0,1]
	v_pk_fma_f32 v[14:15], v[192:193], v[220:221], v[14:15] op_sel_hi:[1,0,1]
	v_pk_fma_f32 v[22:23], v[190:191], v[220:221], v[22:23] op_sel_hi:[1,0,1]
	v_pk_fma_f32 v[166:167], v[190:191], v[230:231], v[166:167] op_sel_hi:[1,0,1]
	v_pk_fma_f32 v[168:169], v[192:193], v[230:231], v[168:169] op_sel_hi:[1,0,1]
	v_pk_fma_f32 v[16:17], v[164:165], v[222:223], v[12:13] op_sel_hi:[1,0,1]
	v_pk_fma_f32 v[26:27], v[162:163], v[222:223], v[24:25] op_sel_hi:[1,0,1]
	v_pk_fma_f32 v[14:15], v[164:165], v[224:225], v[14:15] op_sel_hi:[1,0,1]
	v_pk_fma_f32 v[24:25], v[162:163], v[224:225], v[22:23] op_sel_hi:[1,0,1]
	v_pk_fma_f32 v[12:13], v[164:165], v[232:233], v[168:169] op_sel_hi:[1,0,1]
	v_pk_fma_f32 v[22:23], v[162:163], v[232:233], v[166:167] op_sel_hi:[1,0,1]
.Lmod_done:
	v_mbcnt_lo_u32_b32 v1, -1, 0
	v_mbcnt_hi_u32_b32 v1, -1, v1
	v_and_b32_e32 v2, 64, v1
	v_add_u32_e32 v5, 64, v2
	v_xor_b32_e32 v2, 8, v1
	v_cmp_lt_i32_e32 vcc, v2, v5
	v_xor_b32_e32 v3, 16, v1
	v_xor_b32_e32 v7, 32, v1
	v_cndmask_b32_e32 v2, v1, v2, vcc
	v_cmp_lt_i32_e32 vcc, v3, v5
	v_lshlrev_b32_e32 v28, 2, v2
	ds_bpermute_b32 v4, v28, v22
	v_cndmask_b32_e32 v3, v1, v3, vcc
	v_cmp_lt_i32_e32 vcc, v7, v5
	ds_bpermute_b32 v6, v28, v24
	ds_bpermute_b32 v5, v28, v23
	v_cndmask_b32_e32 v1, v1, v7, vcc
	ds_bpermute_b32 v7, v28, v25
	v_lshlrev_b32_e32 v31, 2, v3
	ds_bpermute_b32 v2, v28, v26
	s_waitcnt lgkmcnt(2)
	v_pk_add_f32 v[18:19], v[22:23], v[4:5]
	ds_bpermute_b32 v3, v28, v27
	s_waitcnt lgkmcnt(2)
	v_pk_add_f32 v[22:23], v[24:25], v[6:7]
	ds_bpermute_b32 v20, v31, v18
	ds_bpermute_b32 v21, v31, v19
	ds_bpermute_b32 v24, v31, v22
	ds_bpermute_b32 v25, v31, v23
	s_waitcnt lgkmcnt(4)
	v_pk_add_f32 v[2:3], v[26:27], v[2:3]
	ds_bpermute_b32 v26, v28, v14
	s_waitcnt lgkmcnt(3)
	v_pk_add_f32 v[6:7], v[18:19], v[20:21]
	ds_bpermute_b32 v27, v28, v15
	s_waitcnt lgkmcnt(2)
	v_pk_add_f32 v[18:19], v[22:23], v[24:25]
	ds_bpermute_b32 v22, v28, v16
	ds_bpermute_b32 v23, v28, v17
	ds_bpermute_b32 v24, v28, v12
	ds_bpermute_b32 v25, v28, v13
	s_waitcnt lgkmcnt(4)
	v_pk_add_f32 v[26:27], v[14:15], v[26:27]
	ds_bpermute_b32 v8, v31, v2
	s_waitcnt lgkmcnt(3)
	v_pk_add_f32 v[16:17], v[16:17], v[22:23]
	ds_bpermute_b32 v9, v31, v3
	s_waitcnt lgkmcnt(2)
	v_pk_add_f32 v[24:25], v[12:13], v[24:25]
	ds_bpermute_b32 v22, v31, v16
	ds_bpermute_b32 v23, v31, v17
	ds_bpermute_b32 v28, v31, v24
	ds_bpermute_b32 v29, v31, v25
	ds_bpermute_b32 v30, v31, v26
	ds_bpermute_b32 v31, v31, v27
	v_lshlrev_b32_e32 v1, 2, v1
	s_waitcnt lgkmcnt(6)
	v_pk_add_f32 v[2:3], v[2:3], v[8:9]
	s_waitcnt lgkmcnt(4)
	v_pk_add_f32 v[12:13], v[16:17], v[22:23]
	s_waitcnt lgkmcnt(2)
	v_pk_add_f32 v[16:17], v[24:25], v[28:29]
	s_waitcnt lgkmcnt(0)
	v_pk_add_f32 v[24:25], v[26:27], v[30:31]
	ds_bpermute_b32 v4, v1, v2
	ds_bpermute_b32 v8, v1, v6
	ds_bpermute_b32 v20, v1, v18
	ds_bpermute_b32 v5, v1, v3
	ds_bpermute_b32 v9, v1, v7
	ds_bpermute_b32 v21, v1, v19
	ds_bpermute_b32 v14, v1, v12
	ds_bpermute_b32 v22, v1, v16
	ds_bpermute_b32 v26, v1, v24
	ds_bpermute_b32 v15, v1, v13
	ds_bpermute_b32 v23, v1, v17
	ds_bpermute_b32 v27, v1, v25
	v_cmp_gt_u32_e32 vcc, 8, v254
	s_and_saveexec_b64 s[0:1], vcc
	s_cbranch_execz .LBB0_283
	v_lshl_add_u64 v[28:29], s[22:23], 0, v[10:11]
	global_load_dwordx4 v[28:31], v[28:29], off
	s_waitcnt lgkmcnt(8)
	v_pk_add_f32 v[2:3], v[2:3], v[4:5]
	v_lshl_add_u64 v[4:5], s[50:51], 0, v[10:11]
	s_mov_b32 s2, 0x110000
	s_waitcnt lgkmcnt(7)
	v_pk_add_f32 v[6:7], v[6:7], v[8:9]
	s_waitcnt lgkmcnt(2)
	v_pk_add_f32 v[8:9], v[12:13], v[14:15]
	v_add_co_u32_e32 v14, vcc, s2, v4
	s_mov_b32 s3, 0x11c000
	s_nop 0
	v_addc_co_u32_e32 v15, vcc, 0, v5, vcc
	v_pk_add_f32 v[18:19], v[18:19], v[20:21]
	v_add_co_u32_e32 v20, vcc, s3, v4
	s_waitcnt lgkmcnt(1)
	v_pk_add_f32 v[16:17], v[16:17], v[22:23]
	v_addc_co_u32_e32 v21, vcc, 0, v5, vcc
	v_add_co_u32_e32 v22, vcc, 0x128000, v4
	s_waitcnt lgkmcnt(0)
	v_pk_add_f32 v[24:25], v[24:25], v[26:27]
	v_addc_co_u32_e32 v23, vcc, 0, v5, vcc
	s_waitcnt vmcnt(0)
	v_pk_add_f32 v[2:3], v[2:3], v[28:29]
	v_pk_add_f32 v[4:5], v[8:9], v[30:31]
	v_pk_add_f32 v[6:7], v[6:7], v[28:29]
	v_pk_add_f32 v[8:9], v[16:17], v[30:31]
	v_pk_add_f32 v[10:11], v[18:19], v[28:29]
	v_pk_add_f32 v[12:13], v[24:25], v[30:31]
	global_store_dwordx4 v[14:15], v[2:5], off
	global_store_dwordx4 v[20:21], v[6:9], off
	global_store_dwordx4 v[22:23], v[10:13], off
